# rw state phase W/Y/S stages: LDS fragment reads issued up front; last-layer final grid barrier skipped
# speedup vs baseline: 1.0138x; 1.0003x over previous
; #define LAS __attribute__((address_space(3)))
; __device__ __forceinline__ void rwkv_state_phase(LAS unsigned char* lds, const unsigned char* img, bf16_t* y_, const RwScan& a_, const int vcu, const int G, const int tid0_) {
;     ...
;             {
;                 const int mt = wave >> 1, nt = wave & 1;
;                 const f32x4 pl = *(const LAS f32x4*)(PL + 16 * mt + 4 * fq);
;                 Sacc = __builtin_amdgcn_mfma_f32_16x16x32_bf16(ldfrag(BhT, P32, 16 * mt + fr, 8 * fq), ldfrag(Ui, P32, 16 * nt + fr, 8 * fq), Sacc, 0, 0, 0);
;                 Sacc = __builtin_amdgcn_mfma_f32_16x16x32_bf16(ldfrag(KhT, P32, 16 * mt + fr, 8 * fq), ldfrag(Vi, P32, 16 * nt + fr, 8 * fq), Sacc, 0, 0, 0);
;                 Sacc = Sacc * pl;
;             }
.LBB0_746:
	s_lshl_b32 s34, s18, 2
	s_add_i32 s34, s65, s34
	v_lshlrev_b32_e32 v2, 1, v2
	v_lshlrev_b32_e32 v5, 1, v5
	v_lshl_add_u32 v79, v97, 2, s34
	v_lshlrev_b32_e32 v4, 1, v4
	v_add3_u32 v2, s65, v2, v5
	v_add3_u32 v114, 0, v4, v5
	v_add3_u32 v115, s65, v4, v5
	ds_read_b128 v[94:97], v79 offset:41984
	ds_read_b128 v[98:101], v2 offset:31744
	ds_read_b128 v[102:105], v114 offset:29184
	ds_read_b128 v[160:163], v2 offset:36864
	ds_read_b128 v[164:167], v115 offset:24064
	s_add_i32 s33, s33, 32
	s_waitcnt lgkmcnt(2)
	v_mfma_f32_16x16x32_bf16 v[62:65], v[98:101], v[102:105], v[62:65]
	s_add_u32 s28, s28, 0x7100
	s_waitcnt lgkmcnt(0)
	v_mfma_f32_16x16x32_bf16 v[62:65], v[160:163], v[164:167], v[62:65]
	s_addc_u32 s29, s29, 0
	s_add_i32 s64, s64, 1
	s_cmp_eq_u32 s28, 0x1bcf00
	s_nop 4
	v_pk_mul_f32 v[64:65], v[96:97], v[64:65]
	v_pk_mul_f32 v[62:63], v[94:95], v[62:63]
	s_cbranch_scc1 .LBB0_806

; #define LAS __attribute__((address_space(3)))
; __device__ __forceinline__ unsigned cvt_pk_bf16(float lo, float hi) { const f32x2 v = {lo, hi}; const bf16x2_t b = __builtin_convertvector(v, bf16x2_t); return __builtin_bit_cast(unsigned, b); }
; #define ZERO4() ((f32x4){opaque0(), 0.f, 0.f, 0.f} * 0.f)
; __device__ __forceinline__ void rwkv_state_phase(LAS unsigned char* lds, const unsigned char* img, bf16_t* y_, const RwScan& a_, const int vcu, const int G, const int tid0_) {
;     ...
;             if (wave >= 4) {
;                 const int mt = (wave - 4) >> 1, nt = (wave - 4) & 1;
;                 f32x4 w = ZERO4();
; #pragma unroll
;                 for (int ks = 0; ks < 2; ++ks) w = __builtin_amdgcn_mfma_f32_16x16x32_bf16(ldfrag(AT, P64, 16 * mt + fr, 32 * ks + 8 * fq), ldfrag(S0, P64, 16 * nt + fr, 32 * ks + 8 * fq), w, 0, 0, 0);
;                 w = __builtin_amdgcn_mfma_f32_16x16x32_bf16(ldfrag(NakT, P32, 16 * mt + fr, 8 * fq), ldfrag(Vi, P32, 16 * nt + fr, 8 * fq), w, 0, 0, 0);
;                 u32x2 o; o.x = cvt_pk_bf16(w[0], w[1]); o.y = cvt_pk_bf16(w[2], w[3]); *(LAS u32x2*)(Wi + (16 * nt + fr) * P32 + 16 * mt + 4 * fq) = o;
;             }
.LBB0_763:
	v_lshlrev_b32_e32 v97, 2, v96
	v_cndmask_b32_e64 v4, 0, 1, s[16:17]
	v_lshlrev_b32_e32 v99, 4, v96
	v_cmp_ne_u32_e64 s[10:11], 1, v4
	s_andn2_b64 vcc, exec, s[16:17]
	v_mul_u32_u24_e32 v101, 0x50, v95
	v_lshlrev_b32_e32 v94, 1, v97
	v_add_u32_e32 v98, v2, v99
	s_cbranch_vccnz .LBB0_765
	v_or_b32_e32 v100, s55, v81
	v_mul_lo_u32 v102, v100, s67
	v_mov_b32_e32 v2, v3
	v_add3_u32 v110, s65, v102, v99
	v_mul_lo_u32 v114, v100, s66
	v_add3_u32 v115, s65, v101, v99
	v_add3_u32 v114, s65, v114, v99
	ds_read_b128 v[102:105], v110
	ds_read_b128 v[106:109], v98 offset:9216
	ds_read_b128 v[160:163], v110 offset:64
	ds_read_b128 v[164:167], v98 offset:9280
	ds_read_b128 v[168:171], v114 offset:13824
	ds_read_b128 v[172:175], v115 offset:24064
	v_mul_f32_e32 v2, 0, v2
	v_mov_b32_e32 v4, v3
	v_mov_b32_e32 v5, v3
	s_waitcnt lgkmcnt(4)
	s_nop 0
	v_mfma_f32_16x16x32_bf16 v[102:105], v[102:105], v[106:109], v[2:5]
	s_waitcnt lgkmcnt(2)
	v_mfma_f32_16x16x32_bf16 v[102:105], v[160:163], v[164:167], v[102:105]
	s_waitcnt lgkmcnt(0)
	v_mfma_f32_16x16x32_bf16 v[102:105], v[168:171], v[172:175], v[102:105]
	v_add3_u32 v2, s56, v101, v94
	s_nop 7
	v_cvt_pk_bf16_f32 v4, v102, v103
	v_cvt_pk_bf16_f32 v5, v104, v105
	ds_write_b64 v2, v[4:5] offset:26560

; __device__ __forceinline__ unsigned cvt_pk_bf16(float lo, float hi) { const f32x2 v = {lo, hi}; const bf16x2_t b = __builtin_convertvector(v, bf16x2_t); return __builtin_bit_cast(unsigned, b); }
; #define ZERO4() ((f32x4){opaque0(), 0.f, 0.f, 0.f} * 0.f)
; __device__ __forceinline__ void rwkv_state_phase(LAS unsigned char* lds, const unsigned char* img, bf16_t* y_, const RwScan& a_, const int vcu, const int G, const int tid0_) {
;     ...
;             if (wave < 4) {
;                 const int mt = wave >> 1, nt = wave & 1;
;                 f32x4 y = ZERO4();
; #pragma unroll
;                 for (int ks = 0; ks < 2; ++ks) y = __builtin_amdgcn_mfma_f32_16x16x32_bf16(ldfrag(S0, P64, 16 * mt + fr, 32 * ks + 8 * fq), ldfrag(RT, P64, 16 * nt + fr, 32 * ks + 8 * fq), y, 0, 0, 0);
;                 y = __builtin_amdgcn_mfma_f32_16x16x32_bf16(ldfrag(Ui, P32, 16 * mt + fr, 8 * fq), ldfrag(MbrT, P32, 16 * nt + fr, 8 * fq), y, 0, 0, 0);
;                 y = __builtin_amdgcn_mfma_f32_16x16x32_bf16(ldfrag(Vi, P32, 16 * mt + fr, 8 * fq), ldfrag(MkrT, P32, 16 * nt + fr, 8 * fq), y, 0, 0, 0);
;                 u32x2 o; o.x = cvt_pk_bf16(y[0], y[1]); o.y = cvt_pk_bf16(y[2], y[3]);
;                 *(u32x2*)(y_ + (size_t)(b * SEQ + t0 + 16 * nt + fr) * 1024 + h * 64 + half * 32 + 16 * mt + 4 * fq) = o;
;             }
.LBB0_804:
	s_andn2_b64 vcc, exec, s[34:35]
	s_cbranch_vccnz .LBB0_746
	v_mul_lo_u32 v96, v100, s67
	v_mov_b32_e32 v2, v3
	v_add3_u32 v96, s65, v96, v99
	v_mul_lo_u32 v114, v100, 40
	v_lshlrev_b32_e32 v116, 6, v95
	v_lshlrev_b32_e32 v117, 6, v100
	v_lshlrev_b32_e32 v115, 1, v114
	v_sub_u32_e32 v116, v98, v116
	v_sub_u32_e32 v117, v96, v117
	v_add3_u32 v115, 0, v115, v99
	ds_read_b128 v[102:105], v96 offset:9216
	ds_read_b128 v[106:109], v98 offset:4608
	ds_read_b128 v[160:163], v96 offset:9280
	ds_read_b128 v[164:167], v98 offset:4672
	ds_read_b128 v[168:171], v115 offset:29184
	ds_read_b128 v[172:175], v116 offset:16384
	ds_read_b128 v[176:179], v117 offset:24064
	ds_read_b128 v[180:183], v116 offset:18944
	v_mul_f32_e32 v2, 0, v2
	v_mov_b32_e32 v4, v3
	v_mov_b32_e32 v5, v3
	s_waitcnt lgkmcnt(6)
	s_nop 0
	v_mfma_f32_16x16x32_bf16 v[102:105], v[102:105], v[106:109], v[2:5]
	v_add_u32_e32 v98, s33, v81
	v_ashrrev_i32_e32 v99, 31, v98
	s_waitcnt lgkmcnt(4)
	v_mfma_f32_16x16x32_bf16 v[102:105], v[160:163], v[164:167], v[102:105]
	s_waitcnt lgkmcnt(2)
	v_mfma_f32_16x16x32_bf16 v[102:105], v[168:171], v[172:175], v[102:105]
	v_mov_b32_e32 v2, v114
	s_waitcnt lgkmcnt(0)
	v_mfma_f32_16x16x32_bf16 v[102:105], v[176:179], v[180:183], v[102:105]
	v_lshlrev_b64 v[98:99], 11, v[98:99]
	v_lshl_add_u64 v[98:99], s[2:3], 0, v[98:99]
	v_mov_b32_e32 v95, v3
	s_nop 4
	v_cvt_pk_bf16_f32 v4, v102, v103
	v_cvt_pk_bf16_f32 v5, v104, v105
	v_lshl_add_u64 v[94:95], v[98:99], 0, v[94:95]
	global_store_dwordx2 v[94:95], v[4:5], off
	v_mov_b32_e32 v4, v101
	v_mov_b32_e32 v5, v79
	s_branch .LBB0_746

; #define SEAM(k) do { if (((k) & 15) == 3 && TS_ON(21)) { TS_END(21); } if ((k) + 1 < hi) { TS_END((k) & 15); TS_BEGIN(20); xcd_barrier(bar); if ((MK_DBL >> 19) & 1) xcd_barrier(bar); TS_END(20); } else { TS_END((k) & 15); } } while (0)
; __global__ void __launch_bounds__(NWAVES * 64, 2) fwd(Params P) {
;     ...
;             }
;             SEAM(pb + 10);
;         }
;     }
.LBB0_1870:
	v_readlane_b32 s14, v254, 7
	v_readlane_b32 s15, v254, 8
	s_cmp_eq_u32 s14, 3
	s_cbranch_scc1 .Lskip_final_barrier
	s_waitcnt vmcnt(0)
	s_barrier
	s_mov_b64 s[2:3], exec
	v_readlane_b32 s4, v253, 7
	v_readlane_b32 s5, v253, 8
	s_and_b64 s[4:5], s[2:3], s[4:5]
	s_mov_b64 s[36:37], 0x3fffff
	s_mov_b64 exec, s[4:5]
	s_cbranch_execnz .LBB0_1871
.Lskip_final_barrier:
	s_getpc_b64 s[98:99]
